# phase 12 row loop: TOPI/TRANK of the next row prefetched one iteration ahead, TOPW no longer waited for before the expert-output gather loads; on top of v43
# baseline (speedup 1.0000x reference)
; #define GAS __attribute__((address_space(1)))
; __device__ __forceinline__ void phase12(KP kp, LAS unsigned char* lds, int wave, int bid, int G) {
;     ...
;     for (int m = bid * NWAVES + wave; m < T; m += G * NWAVES) {
;         const GAS f32x4* xr = (const GAS f32x4*)(X1 + (size_t)m * DM) + lane;
;         const i32x4 te = *(const GAS i32x4*)(TOPI + m * 4), rk = *(const GAS i32x4*)(TRANK + m * 4); const f32x4 tw = *(const GAS f32x4*)(TOPW + m * 4);
;         const i32x4 sl = (i32x4){pstart[te.x] + rk.x, pstart[te.y] + rk.y, pstart[te.z] + rk.z, pstart[te.w] + rk.w};
;         const GAS u32x2* y0 = (const GAS u32x2*)(YS + (size_t)sl.x * DM) + lane; const GAS u32x2* y1 = (const GAS u32x2*)(YS + (size_t)sl.y * DM) + lane;
;         const GAS u32x2* y2 = (const GAS u32x2*)(YS + (size_t)sl.z * DM) + lane; const GAS u32x2* y3 = (const GAS u32x2*)(YS + (size_t)sl.w * DM) + lane;
.LBB0_4680:
	s_lshl_b32 s2, s81, 3
	s_add_i32 s2, s82, s2
	s_cmpk_gt_i32 s2, 0x1fff
	s_waitcnt vmcnt(0)
	v_mbcnt_lo_u32_b32 v0, -1, 0
	v_mbcnt_hi_u32_b32 v0, -1, v0
	s_cbranch_scc1 .LBB0_4683
	s_load_dwordx2 s[12:13], s[0:1], 0xc8
	s_load_dwordx4 s[8:11], s[0:1], 0xb8
	s_waitcnt lgkmcnt(0)
	v_mbcnt_lo_u32_b32 v6, -1, 0
	v_ashrrev_i32_e32 v1, 31, v0
	v_mbcnt_hi_u32_b32 v6, -1, v6
	v_lshl_add_u64 v[2:3], v[0:1], 3, s[12:13]
	s_mov_b64 s[0:1], 0x6e000000
	v_and_b32_e32 v7, 64, v6
	v_lshl_add_u64 v[68:69], v[2:3], 0, s[0:1]
	v_lshlrev_b32_e32 v2, 2, v0
	v_add_u32_e32 v7, 64, v7
	v_xor_b32_e32 v8, 1, v6
	v_ashrrev_i32_e32 v3, 31, v2
	v_cmp_lt_i32_e32 vcc, v8, v7
	v_lshlrev_b64 v[2:3], 2, v[2:3]
	v_lshl_add_u64 v[4:5], s[12:13], 0, v[2:3]
	v_cndmask_b32_e32 v8, v6, v8, vcc
	s_mov_b64 s[0:1], 0x20a000
	v_lshlrev_b32_e32 v94, 2, v8
	v_xor_b32_e32 v8, 2, v6
	v_lshl_add_u64 v[70:71], v[4:5], 0, s[0:1]
	v_cmp_lt_i32_e32 vcc, v8, v7
	s_mov_b64 s[0:1], 0x20b000
	v_lshl_add_u64 v[74:75], v[4:5], 0, s[0:1]
	v_cndmask_b32_e32 v8, v6, v8, vcc
	s_mov_b64 s[0:1], 0x20b400
	v_lshlrev_b32_e32 v95, 2, v8
	v_xor_b32_e32 v8, 4, v6
	v_lshl_add_u64 v[76:77], v[4:5], 0, s[0:1]
	s_mov_b64 s[0:1], 0x20b800
	s_add_u32 s14, s12, 0x500000
	v_cmp_lt_i32_e32 vcc, v8, v7
	v_lshl_add_u64 v[78:79], v[4:5], 0, s[0:1]
	s_mov_b64 s[0:1], 0x20bc00
	s_addc_u32 s15, s13, 0
	v_cndmask_b32_e32 v8, v6, v8, vcc
	v_lshl_add_u64 v[72:73], s[8:9], 0, v[2:3]
	v_lshl_add_u64 v[80:81], v[4:5], 0, s[0:1]
	s_mov_b64 s[0:1], 0x1000
	s_add_u32 s17, s12, 0x580000
	v_lshlrev_b32_e32 v96, 2, v8
	v_xor_b32_e32 v8, 8, v6
	v_lshl_add_u64 v[82:83], v[72:73], 0, s[0:1]
	s_mov_b64 s[0:1], 0x1400
	s_addc_u32 s18, s13, 0
	v_cmp_lt_i32_e32 vcc, v8, v7
	v_lshl_add_u64 v[84:85], v[72:73], 0, s[0:1]
	s_mov_b64 s[0:1], 0x1800
	s_add_u32 s19, s12, 0x540000
	v_cndmask_b32_e32 v8, v6, v8, vcc
	v_lshl_add_u64 v[86:87], v[72:73], 0, s[0:1]
	s_mov_b64 s[0:1], 0x1c00
	s_addc_u32 s20, s13, 0
	v_lshlrev_b32_e32 v97, 2, v8
	v_xor_b32_e32 v8, 16, v6
	v_lshl_add_u64 v[88:89], v[72:73], 0, s[0:1]
	s_lshl_b32 s0, s81, 5
	s_lshl_b32 s1, s82, 2
	s_ashr_i32 s3, s2, 31
	s_lshl_b32 s6, s16, 3
	v_cmp_lt_i32_e32 vcc, v8, v7
	s_add_i32 s4, s0, s1
	s_lshl_b32 s16, s16, 5
	s_lshl_b64 s[0:1], s[2:3], 13
	v_cndmask_b32_e32 v8, v6, v8, vcc
	s_add_u32 s8, s10, s0
	v_lshlrev_b32_e32 v98, 2, v8
	v_xor_b32_e32 v8, 32, v6
	s_addc_u32 s9, s11, s1
	s_ashr_i32 s7, s6, 31
	v_cmp_lt_i32_e32 vcc, v8, v7
	s_lshl_b64 s[10:11], s[6:7], 13
	s_add_u32 s12, s12, s0
	v_cndmask_b32_e32 v6, v6, v8, vcc
	v_lshlrev_b32_e32 v99, 2, v6
	v_lshlrev_b64 v[90:91], 4, v[0:1]
	s_addc_u32 s13, s13, s1
	v_mov_b32_e32 v100, 0
	s_add_i32 s3, 0, 0x27000
	s_mov_b32 s7, 0x56000000
	s_mov_b32 s21, 0x56001000
	v_mov_b32_e32 v101, 0x3727c5ac
	s_mov_b32 s22, 0xf800000
	v_mov_b32_e32 v102, 0x260
	s_movk_i32 s23, 0x1000
	s_ashr_i32 s5, s4, 31
	s_lshl_b64 s[0:1], s[4:5], 2
	s_add_u32 s24, s14, s0
	s_addc_u32 s25, s15, s1
	global_load_dwordx4 v[238:241], v100, s[24:25]
	s_add_u32 s24, s17, s0
	s_addc_u32 s25, s18, s1
	global_load_dwordx4 v[242:245], v100, s[24:25]
	v_lshl_add_u64 v[36:37], s[12:13], 0, v[90:91]
	s_ashr_i32 s5, s4, 31
	v_add_co_u32_e32 v104, vcc, s7, v36
	s_lshl_b64 s[0:1], s[4:5], 2
	s_nop 0
	v_addc_co_u32_e32 v105, vcc, 0, v37, vcc
	v_add_co_u32_e32 v106, vcc, s21, v36
	s_nop 0
	v_addc_co_u32_e32 v107, vcc, 0, v37, vcc
	global_load_dwordx4 v[0:3], v[70:71], off
	global_load_dwordx4 v[4:7], v[70:71], off offset:1024
	global_load_dwordx4 v[8:11], v[70:71], off offset:2048
	global_load_dwordx4 v[12:15], v[70:71], off offset:3072
	global_load_dwordx4 v[16:19], v[74:75], off
	global_load_dwordx4 v[20:23], v[76:77], off
	global_load_dwordx4 v[24:27], v[78:79], off
	global_load_dwordx4 v[32:35], v[80:81], off
	global_load_dwordx4 v[28:31], v[72:73], off
	global_load_dwordx4 v[60:63], v[104:105], off offset:1024
	global_load_dwordx4 v[56:59], v[104:105], off offset:2048
	global_load_dwordx4 v[48:51], v[104:105], off offset:3072
	global_load_dwordx4 v[64:67], v[106:107], off offset:-4096
	global_load_dwordx4 v[52:55], v[106:107], off
	global_load_dwordx4 v[44:47], v[106:107], off offset:1024
	global_load_dwordx4 v[40:43], v[106:107], off offset:2048
	global_load_dwordx4 v[36:39], v[106:107], off offset:3072
	v_lshl_add_u64 v[92:93], s[8:9], 0, v[90:91]
	s_add_u32 s0, s19, s0
	s_addc_u32 s1, s20, s1
	global_load_dwordx4 v[112:115], v100, s[0:1]
	s_waitcnt vmcnt(18)
	s_branch .Lp12_mid
.LBB0_4682:
	v_lshl_add_u64 v[36:37], s[12:13], 0, v[90:91]
	s_ashr_i32 s5, s4, 31
	v_add_co_u32_e32 v104, vcc, s7, v36
	s_lshl_b64 s[0:1], s[4:5], 2
	s_nop 0
	v_addc_co_u32_e32 v105, vcc, 0, v37, vcc
	v_add_co_u32_e32 v106, vcc, s21, v36
	s_nop 0
	v_addc_co_u32_e32 v107, vcc, 0, v37, vcc
	global_load_dwordx4 v[0:3], v[70:71], off
	global_load_dwordx4 v[4:7], v[70:71], off offset:1024
	global_load_dwordx4 v[8:11], v[70:71], off offset:2048
	global_load_dwordx4 v[12:15], v[70:71], off offset:3072
	global_load_dwordx4 v[16:19], v[74:75], off
	global_load_dwordx4 v[20:23], v[76:77], off
	global_load_dwordx4 v[24:27], v[78:79], off
	global_load_dwordx4 v[32:35], v[80:81], off
	global_load_dwordx4 v[28:31], v[72:73], off
	global_load_dwordx4 v[60:63], v[104:105], off offset:1024
	global_load_dwordx4 v[56:59], v[104:105], off offset:2048
	global_load_dwordx4 v[48:51], v[104:105], off offset:3072
	global_load_dwordx4 v[64:67], v[106:107], off offset:-4096
	global_load_dwordx4 v[52:55], v[106:107], off
	global_load_dwordx4 v[44:47], v[106:107], off offset:1024
	global_load_dwordx4 v[40:43], v[106:107], off offset:2048
	global_load_dwordx4 v[36:39], v[106:107], off offset:3072
	v_lshl_add_u64 v[92:93], s[8:9], 0, v[90:91]
	s_add_u32 s0, s19, s0
	s_addc_u32 s1, s20, s1
	global_load_dwordx4 v[112:115], v100, s[0:1]
; #define GAS __attribute__((address_space(1)))
; __device__ __forceinline__ void phase12(KP kp, LAS unsigned char* lds, int wave, int bid, int G) {
;     ...
;         const i32x4 te = *(const GAS i32x4*)(TOPI + m * 4), rk = *(const GAS i32x4*)(TRANK + m * 4); const f32x4 tw = *(const GAS f32x4*)(TOPW + m * 4);
;         const i32x4 sl = (i32x4){pstart[te.x] + rk.x, pstart[te.y] + rk.y, pstart[te.z] + rk.z, pstart[te.w] + rk.w};
;         const GAS u32x2* y0 = (const GAS u32x2*)(YS + (size_t)sl.x * DM) + lane; const GAS u32x2* y1 = (const GAS u32x2*)(YS + (size_t)sl.y * DM) + lane;
;         const GAS u32x2* y2 = (const GAS u32x2*)(YS + (size_t)sl.z * DM) + lane; const GAS u32x2* y3 = (const GAS u32x2*)(YS + (size_t)sl.w * DM) + lane;
.Lp12_mid:
	v_mov_b32_e32 v104, v238
	v_mov_b32_e32 v105, v239
	v_mov_b32_e32 v106, v240
	v_mov_b32_e32 v107, v241
	v_mov_b32_e32 v108, v242
	v_mov_b32_e32 v109, v243
	v_mov_b32_e32 v110, v244
	v_mov_b32_e32 v111, v245
	s_add_i32 s2, s2, s6
	s_add_i32 s4, s4, s16
	s_add_u32 s8, s8, s10
	s_addc_u32 s9, s9, s11
	s_add_u32 s12, s12, s10
	s_addc_u32 s13, s13, s11
	s_cmpk_lt_i32 s2, 0x2000
	s_cbranch_scc0 .Lp12_nopf
	s_ashr_i32 s5, s4, 31
	s_lshl_b64 s[0:1], s[4:5], 2
	s_add_u32 s24, s14, s0
	s_addc_u32 s25, s15, s1
	global_load_dwordx4 v[238:241], v100, s[24:25]
	s_add_u32 s24, s17, s0
	s_addc_u32 s25, s18, s1
	global_load_dwordx4 v[242:245], v100, s[24:25]
.Lp12_nopf:
	s_cmpk_lt_i32 s2, 0x2000
	v_lshlrev_b32_e32 v103, 2, v104
	v_lshlrev_b32_e32 v104, 2, v105
	v_lshlrev_b32_e32 v105, 2, v106
	v_lshlrev_b32_e32 v106, 2, v107
	v_add_u32_e32 v103, s3, v103
	v_add_u32_e32 v105, s3, v105
	v_add_u32_e32 v104, s3, v104
	v_add_u32_e32 v106, s3, v106
	ds_read_b32 v103, v103
	ds_read_b32 v107, v104
	ds_read_b32 v105, v105
	ds_read_b32 v116, v106
	s_waitcnt lgkmcnt(3)
	v_add_u32_e32 v106, v103, v108
	s_waitcnt lgkmcnt(2)
	v_add_u32_e32 v108, v107, v109
	s_waitcnt lgkmcnt(1)
	v_add_u32_e32 v110, v105, v110
	s_waitcnt lgkmcnt(0)
	v_add_u32_e32 v116, v116, v111
	v_ashrrev_i32_e32 v107, 31, v106
	v_ashrrev_i32_e32 v109, 31, v108
	v_ashrrev_i32_e32 v111, 31, v110
	v_ashrrev_i32_e32 v117, 31, v116
	v_lshlrev_b64 v[106:107], 12, v[106:107]
	v_lshlrev_b64 v[108:109], 12, v[108:109]
	v_lshlrev_b64 v[110:111], 12, v[110:111]
	v_lshlrev_b64 v[116:117], 12, v[116:117]
	v_lshl_add_u64 v[106:107], v[68:69], 0, v[106:107]
	v_lshl_add_u64 v[108:109], v[68:69], 0, v[108:109]
	v_lshl_add_u64 v[110:111], v[68:69], 0, v[110:111]
	v_lshl_add_u64 v[116:117], v[68:69], 0, v[116:117]
	global_load_dwordx2 v[118:119], v[106:107], off
	global_load_dwordx2 v[120:121], v[108:109], off
	global_load_dwordx2 v[122:123], v[110:111], off
	global_load_dwordx2 v[124:125], v[116:117], off
	global_load_dwordx2 v[126:127], v[106:107], off offset:512
	global_load_dwordx2 v[128:129], v[108:109], off offset:512
	global_load_dwordx2 v[130:131], v[110:111], off offset:512
	global_load_dwordx2 v[132:133], v[116:117], off offset:512
	global_load_dwordx2 v[134:135], v[106:107], off offset:1024
	global_load_dwordx2 v[136:137], v[108:109], off offset:1024
	global_load_dwordx2 v[138:139], v[110:111], off offset:1024
	global_load_dwordx2 v[140:141], v[116:117], off offset:1024
	global_load_dwordx2 v[142:143], v[106:107], off offset:1536
	global_load_dwordx2 v[144:145], v[108:109], off offset:1536
	global_load_dwordx2 v[146:147], v[110:111], off offset:1536
	global_load_dwordx2 v[148:149], v[116:117], off offset:1536
	global_load_dwordx2 v[150:151], v[106:107], off offset:2048
	global_load_dwordx2 v[152:153], v[106:107], off offset:2560
	global_load_dwordx2 v[154:155], v[106:107], off offset:3072
	s_nop 0
	global_load_dwordx2 v[106:107], v[106:107], off offset:3584
	s_nop 0
	global_load_dwordx2 v[156:157], v[108:109], off offset:2048
	global_load_dwordx2 v[158:159], v[108:109], off offset:2560
	global_load_dwordx2 v[160:161], v[108:109], off offset:3072
	s_nop 0
	global_load_dwordx2 v[108:109], v[108:109], off offset:3584
	s_nop 0
	global_load_dwordx2 v[162:163], v[110:111], off offset:2048
	global_load_dwordx2 v[164:165], v[110:111], off offset:2560
	global_load_dwordx2 v[166:167], v[110:111], off offset:3072
	s_nop 0
	global_load_dwordx2 v[110:111], v[110:111], off offset:3584
	s_nop 0
	global_load_dwordx2 v[168:169], v[116:117], off offset:2048
	global_load_dwordx2 v[170:171], v[116:117], off offset:2560
	global_load_dwordx2 v[172:173], v[116:117], off offset:3072
	s_nop 0
	global_load_dwordx2 v[116:117], v[116:117], off offset:3584
	s_waitcnt vmcnt(31)
	v_mov_b32_e32 v104, v115
	v_lshlrev_b32_e32 v174, 16, v118
	s_waitcnt vmcnt(30)
	v_lshlrev_b32_e32 v176, 16, v120
	v_and_b32_e32 v177, 0xffff0000, v120
	v_lshlrev_b32_e32 v120, 16, v121
	v_and_b32_e32 v121, 0xffff0000, v121
	s_waitcnt vmcnt(26)
	v_lshlrev_b32_e32 v184, 16, v128
	v_and_b32_e32 v185, 0xffff0000, v128
	v_lshlrev_b32_e32 v128, 16, v129
	v_and_b32_e32 v129, 0xffff0000, v129
	v_and_b32_e32 v175, 0xffff0000, v118
	v_lshlrev_b32_e32 v118, 16, v119
	v_and_b32_e32 v119, 0xffff0000, v119
	v_lshlrev_b32_e32 v182, 16, v126
	v_and_b32_e32 v183, 0xffff0000, v126
	v_lshlrev_b32_e32 v126, 16, v127
	v_and_b32_e32 v127, 0xffff0000, v127
	s_waitcnt vmcnt(22)
	v_lshlrev_b32_e32 v192, 16, v136
	v_and_b32_e32 v193, 0xffff0000, v136
	v_lshlrev_b32_e32 v136, 16, v137
	v_and_b32_e32 v137, 0xffff0000, v137
	s_waitcnt vmcnt(18)
	v_lshlrev_b32_e32 v200, 16, v144
	v_and_b32_e32 v201, 0xffff0000, v144
	v_lshlrev_b32_e32 v144, 16, v145
	v_and_b32_e32 v145, 0xffff0000, v145
	s_waitcnt vmcnt(11)
	v_lshlrev_b32_e32 v208, 16, v156
	v_and_b32_e32 v209, 0xffff0000, v156
	v_lshlrev_b32_e32 v156, 16, v157
	v_and_b32_e32 v157, 0xffff0000, v157
	s_waitcnt vmcnt(10)
	v_lshlrev_b32_e32 v216, 16, v158
	v_and_b32_e32 v217, 0xffff0000, v158
	v_lshlrev_b32_e32 v158, 16, v159
	v_and_b32_e32 v159, 0xffff0000, v159
	s_waitcnt vmcnt(9)
	v_lshlrev_b32_e32 v224, 16, v160
	v_and_b32_e32 v225, 0xffff0000, v160
	v_lshlrev_b32_e32 v160, 16, v161
	v_and_b32_e32 v161, 0xffff0000, v161
	s_waitcnt vmcnt(8)
; __device__ __forceinline__ f32x4 unpack4(u32x2 w) { return (f32x4){bflo(w.x), bfhi(w.x), bflo(w.y), bfhi(w.y)}; }
; __device__ __forceinline__ void phase12(KP kp, LAS unsigned char* lds, int wave, int bid, int G) {
;     ...
;         for (int j = 0; j < 8; ++j) {
;             const f32x4 mo = tw.x * unpack4(y0[64 * j]) + tw.y * unpack4(y1[64 * j]) + tw.z * unpack4(y2[64 * j]) + tw.w * unpack4(y3[64 * j]);
	v_lshlrev_b32_e32 v232, 16, v108
	v_and_b32_e32 v233, 0xffff0000, v108
	v_lshlrev_b32_e32 v108, 16, v109
	v_and_b32_e32 v109, 0xffff0000, v109
	v_pk_mul_f32 v[120:121], v[112:113], v[120:121] op_sel:[1,0]
	v_pk_mul_f32 v[176:177], v[112:113], v[176:177] op_sel:[1,0]
	v_pk_mul_f32 v[128:129], v[112:113], v[128:129] op_sel:[1,0]
	v_pk_mul_f32 v[184:185], v[112:113], v[184:185] op_sel:[1,0]
	v_lshlrev_b32_e32 v178, 16, v122
	v_and_b32_e32 v179, 0xffff0000, v122
	v_lshlrev_b32_e32 v122, 16, v123
	v_and_b32_e32 v123, 0xffff0000, v123
	v_lshlrev_b32_e32 v186, 16, v130
	v_and_b32_e32 v187, 0xffff0000, v130
	v_lshlrev_b32_e32 v130, 16, v131
	v_and_b32_e32 v131, 0xffff0000, v131
	v_lshlrev_b32_e32 v190, 16, v134
	v_and_b32_e32 v191, 0xffff0000, v134
	v_lshlrev_b32_e32 v134, 16, v135
	v_and_b32_e32 v135, 0xffff0000, v135
	v_lshlrev_b32_e32 v198, 16, v142
	v_and_b32_e32 v199, 0xffff0000, v142
	v_lshlrev_b32_e32 v142, 16, v143
	v_and_b32_e32 v143, 0xffff0000, v143
	v_lshlrev_b32_e32 v206, 16, v150
	v_and_b32_e32 v207, 0xffff0000, v150
	v_lshlrev_b32_e32 v150, 16, v151
	v_and_b32_e32 v151, 0xffff0000, v151
	v_lshlrev_b32_e32 v214, 16, v152
	v_and_b32_e32 v215, 0xffff0000, v152
	v_lshlrev_b32_e32 v152, 16, v153
	v_and_b32_e32 v153, 0xffff0000, v153
	v_lshlrev_b32_e32 v222, 16, v154
	v_and_b32_e32 v223, 0xffff0000, v154
	v_lshlrev_b32_e32 v154, 16, v155
	v_and_b32_e32 v155, 0xffff0000, v155
	v_lshlrev_b32_e32 v230, 16, v106
	v_and_b32_e32 v231, 0xffff0000, v106
	v_lshlrev_b32_e32 v106, 16, v107
	v_and_b32_e32 v107, 0xffff0000, v107
	v_pk_mul_f32 v[192:193], v[112:113], v[192:193] op_sel:[1,0]
	v_pk_mul_f32 v[136:137], v[112:113], v[136:137] op_sel:[1,0]
	v_pk_mul_f32 v[144:145], v[112:113], v[144:145] op_sel:[1,0]
	v_pk_mul_f32 v[200:201], v[112:113], v[200:201] op_sel:[1,0]
	v_pk_mul_f32 v[156:157], v[112:113], v[156:157] op_sel:[1,0]
	v_pk_mul_f32 v[208:209], v[112:113], v[208:209] op_sel:[1,0]
	v_pk_mul_f32 v[216:217], v[112:113], v[216:217] op_sel:[1,0]
	v_pk_mul_f32 v[158:159], v[112:113], v[158:159] op_sel:[1,0]
	v_pk_mul_f32 v[160:161], v[112:113], v[160:161] op_sel:[1,0]
	v_pk_mul_f32 v[224:225], v[112:113], v[224:225] op_sel:[1,0]
	v_pk_mul_f32 v[108:109], v[112:113], v[108:109] op_sel:[1,0]
	v_pk_mul_f32 v[232:233], v[112:113], v[232:233] op_sel:[1,0]
	v_pk_fma_f32 v[174:175], v[112:113], v[174:175], v[176:177] op_sel_hi:[0,1,1]
	v_pk_fma_f32 v[118:119], v[112:113], v[118:119], v[120:121] op_sel_hi:[0,1,1]
	v_pk_fma_f32 v[120:121], v[112:113], v[182:183], v[184:185] op_sel_hi:[0,1,1]
	v_pk_fma_f32 v[126:127], v[112:113], v[126:127], v[128:129] op_sel_hi:[0,1,1]
	v_lshlrev_b32_e32 v180, 16, v124
	v_and_b32_e32 v181, 0xffff0000, v124
	v_lshlrev_b32_e32 v124, 16, v125
	v_and_b32_e32 v125, 0xffff0000, v125
	v_lshlrev_b32_e32 v188, 16, v132
	v_and_b32_e32 v189, 0xffff0000, v132
	v_lshlrev_b32_e32 v132, 16, v133
	v_and_b32_e32 v133, 0xffff0000, v133
	v_lshlrev_b32_e32 v194, 16, v138
	v_and_b32_e32 v195, 0xffff0000, v138
	v_lshlrev_b32_e32 v138, 16, v139
	v_and_b32_e32 v139, 0xffff0000, v139
	v_lshlrev_b32_e32 v202, 16, v146
	v_and_b32_e32 v203, 0xffff0000, v146
	v_lshlrev_b32_e32 v146, 16, v147
	v_and_b32_e32 v147, 0xffff0000, v147
	s_waitcnt vmcnt(7)
	v_lshlrev_b32_e32 v210, 16, v162
	v_and_b32_e32 v211, 0xffff0000, v162
	v_lshlrev_b32_e32 v162, 16, v163
	v_and_b32_e32 v163, 0xffff0000, v163
	s_waitcnt vmcnt(6)
	v_lshlrev_b32_e32 v218, 16, v164
	v_and_b32_e32 v219, 0xffff0000, v164
	v_lshlrev_b32_e32 v164, 16, v165
	v_and_b32_e32 v165, 0xffff0000, v165
	s_waitcnt vmcnt(5)
	v_lshlrev_b32_e32 v226, 16, v166
	v_and_b32_e32 v227, 0xffff0000, v166
	v_lshlrev_b32_e32 v166, 16, v167
	v_and_b32_e32 v167, 0xffff0000, v167
	s_waitcnt vmcnt(4)
	v_lshlrev_b32_e32 v234, 16, v110
	v_and_b32_e32 v235, 0xffff0000, v110
	v_lshlrev_b32_e32 v110, 16, v111
	v_and_b32_e32 v111, 0xffff0000, v111
	v_pk_fma_f32 v[128:129], v[112:113], v[134:135], v[136:137] op_sel_hi:[0,1,1]
	v_pk_fma_f32 v[134:135], v[112:113], v[190:191], v[192:193] op_sel_hi:[0,1,1]
	v_pk_fma_f32 v[136:137], v[112:113], v[198:199], v[200:201] op_sel_hi:[0,1,1]
	v_pk_fma_f32 v[142:143], v[112:113], v[142:143], v[144:145] op_sel_hi:[0,1,1]
	v_pk_fma_f32 v[144:145], v[112:113], v[206:207], v[208:209] op_sel_hi:[0,1,1]
	v_pk_fma_f32 v[150:151], v[112:113], v[150:151], v[156:157] op_sel_hi:[0,1,1]
	v_pk_fma_f32 v[152:153], v[112:113], v[152:153], v[158:159] op_sel_hi:[0,1,1]
	v_pk_fma_f32 v[156:157], v[112:113], v[214:215], v[216:217] op_sel_hi:[0,1,1]
	v_pk_fma_f32 v[158:159], v[112:113], v[222:223], v[224:225] op_sel_hi:[0,1,1]
	v_pk_fma_f32 v[154:155], v[112:113], v[154:155], v[160:161] op_sel_hi:[0,1,1]
	v_pk_fma_f32 v[160:161], v[112:113], v[230:231], v[232:233] op_sel_hi:[0,1,1]
	v_pk_fma_f32 v[106:107], v[112:113], v[106:107], v[108:109] op_sel_hi:[0,1,1]
	v_pk_fma_f32 v[108:109], v[114:115], v[122:123], v[118:119] op_sel_hi:[0,1,1]
	v_pk_fma_f32 v[112:113], v[114:115], v[178:179], v[174:175] op_sel_hi:[0,1,1]
	v_pk_fma_f32 v[118:119], v[114:115], v[130:131], v[126:127] op_sel_hi:[0,1,1]
	v_pk_fma_f32 v[120:121], v[114:115], v[186:187], v[120:121] op_sel_hi:[0,1,1]
	v_lshlrev_b32_e32 v196, 16, v140
	v_and_b32_e32 v197, 0xffff0000, v140
	v_lshlrev_b32_e32 v140, 16, v141
	v_and_b32_e32 v141, 0xffff0000, v141
	v_lshlrev_b32_e32 v204, 16, v148
	v_and_b32_e32 v205, 0xffff0000, v148
	v_lshlrev_b32_e32 v148, 16, v149
	v_and_b32_e32 v149, 0xffff0000, v149
	s_waitcnt vmcnt(3)
	v_lshlrev_b32_e32 v212, 16, v168
	v_and_b32_e32 v213, 0xffff0000, v168
	v_lshlrev_b32_e32 v168, 16, v169
	v_and_b32_e32 v169, 0xffff0000, v169
	s_waitcnt vmcnt(2)
; #define GAS __attribute__((address_space(1)))
; __device__ __forceinline__ float dot4(f32x4 a, f32x4 b) { return (a.x * b.x + a.y * b.y) + (a.z * b.z + a.w * b.w); }
; __device__ __forceinline__ f32x4 unpack4(u32x2 w) { return (f32x4){bflo(w.x), bfhi(w.x), bflo(w.y), bfhi(w.y)}; }
; __device__ __forceinline__ void phase12(KP kp, LAS unsigned char* lds, int wave, int bid, int G) {
;     ...
;             const f32x4 mo = tw.x * unpack4(y0[64 * j]) + tw.y * unpack4(y1[64 * j]) + tw.z * unpack4(y2[64 * j]) + tw.w * unpack4(y3[64 * j]);
;             const f32x4 g2 = *(const GAS f32x4*)(mod + 5 * 2048 + 256 * j + 4 * lane);
;             v[j] = xr[64 * j] + g2 * mo; s += dot4(v[j], v[j]); }
	v_lshlrev_b32_e32 v220, 16, v170
	v_and_b32_e32 v221, 0xffff0000, v170
	v_lshlrev_b32_e32 v170, 16, v171
	v_and_b32_e32 v171, 0xffff0000, v171
	s_waitcnt vmcnt(1)
	v_lshlrev_b32_e32 v228, 16, v172
	v_and_b32_e32 v229, 0xffff0000, v172
	v_lshlrev_b32_e32 v172, 16, v173
	v_and_b32_e32 v173, 0xffff0000, v173
	s_waitcnt vmcnt(0)
	v_lshlrev_b32_e32 v236, 16, v116
	v_and_b32_e32 v237, 0xffff0000, v116
	v_lshlrev_b32_e32 v116, 16, v117
	v_and_b32_e32 v117, 0xffff0000, v117
	v_pk_fma_f32 v[122:123], v[114:115], v[194:195], v[134:135] op_sel_hi:[0,1,1]
	v_pk_fma_f32 v[126:127], v[114:115], v[138:139], v[128:129] op_sel_hi:[0,1,1]
	v_pk_fma_f32 v[128:129], v[114:115], v[146:147], v[142:143] op_sel_hi:[0,1,1]
	v_pk_fma_f32 v[130:131], v[114:115], v[202:203], v[136:137] op_sel_hi:[0,1,1]
	v_pk_fma_f32 v[134:135], v[114:115], v[162:163], v[150:151] op_sel_hi:[0,1,1]
	v_pk_fma_f32 v[136:137], v[114:115], v[210:211], v[144:145] op_sel_hi:[0,1,1]
	v_pk_fma_f32 v[138:139], v[114:115], v[218:219], v[156:157] op_sel_hi:[0,1,1]
	v_pk_fma_f32 v[142:143], v[114:115], v[164:165], v[152:153] op_sel_hi:[0,1,1]
	v_pk_fma_f32 v[144:145], v[114:115], v[166:167], v[154:155] op_sel_hi:[0,1,1]
	v_pk_fma_f32 v[146:147], v[114:115], v[226:227], v[158:159] op_sel_hi:[0,1,1]
	v_pk_fma_f32 v[106:107], v[114:115], v[110:111], v[106:107] op_sel_hi:[0,1,1]
	v_pk_fma_f32 v[110:111], v[114:115], v[234:235], v[160:161] op_sel_hi:[0,1,1]
	v_pk_fma_f32 v[112:113], v[104:105], v[180:181], v[112:113] op_sel_hi:[0,1,1]
	v_pk_fma_f32 v[108:109], v[104:105], v[124:125], v[108:109] op_sel_hi:[0,1,1]
	v_pk_fma_f32 v[114:115], v[104:105], v[188:189], v[120:121] op_sel_hi:[0,1,1]
	v_pk_fma_f32 v[118:119], v[104:105], v[132:133], v[118:119] op_sel_hi:[0,1,1]
	v_pk_fma_f32 v[120:121], v[104:105], v[140:141], v[126:127] op_sel_hi:[0,1,1]
	v_pk_fma_f32 v[122:123], v[104:105], v[196:197], v[122:123] op_sel_hi:[0,1,1]
	v_pk_fma_f32 v[124:125], v[104:105], v[204:205], v[130:131] op_sel_hi:[0,1,1]
	v_pk_fma_f32 v[126:127], v[104:105], v[148:149], v[128:129] op_sel_hi:[0,1,1]
	v_pk_fma_f32 v[128:129], v[104:105], v[212:213], v[136:137] op_sel_hi:[0,1,1]
	v_pk_fma_f32 v[130:131], v[104:105], v[168:169], v[134:135] op_sel_hi:[0,1,1]
	v_pk_fma_f32 v[132:133], v[104:105], v[170:171], v[142:143] op_sel_hi:[0,1,1]
	v_pk_fma_f32 v[134:135], v[104:105], v[220:221], v[138:139] op_sel_hi:[0,1,1]
	v_pk_fma_f32 v[136:137], v[104:105], v[228:229], v[146:147] op_sel_hi:[0,1,1]
	v_pk_fma_f32 v[138:139], v[104:105], v[172:173], v[144:145] op_sel_hi:[0,1,1]
	v_pk_fma_f32 v[110:111], v[104:105], v[236:237], v[110:111] op_sel_hi:[0,1,1]
	v_pk_fma_f32 v[104:105], v[104:105], v[116:117], v[106:107] op_sel_hi:[0,1,1]
	v_pk_fma_f32 v[2:3], v[2:3], v[108:109], v[66:67]
	v_pk_fma_f32 v[0:1], v[0:1], v[112:113], v[64:65]
	v_pk_fma_f32 v[6:7], v[6:7], v[118:119], v[62:63]
	v_pk_fma_f32 v[4:5], v[4:5], v[114:115], v[60:61]
	v_pk_fma_f32 v[8:9], v[8:9], v[122:123], v[56:57]
	v_pk_fma_f32 v[10:11], v[10:11], v[120:121], v[58:59]
	v_pk_fma_f32 v[26:27], v[26:27], v[138:139], v[42:43]
	v_pk_fma_f32 v[34:35], v[34:35], v[104:105], v[38:39]
	v_mov_b32_e32 v38, v1
	v_mov_b32_e32 v39, v5
	v_mov_b32_e32 v42, v3
	v_mov_b32_e32 v43, v7
	v_pk_fma_f32 v[20:21], v[20:21], v[134:135], v[44:45]
	v_pk_fma_f32 v[22:23], v[22:23], v[132:133], v[46:47]
	v_pk_fma_f32 v[24:25], v[24:25], v[136:137], v[40:41]
	v_pk_fma_f32 v[32:33], v[32:33], v[110:111], v[36:37]
	v_mov_b32_e32 v36, v0
	v_mov_b32_e32 v37, v4
	v_mov_b32_e32 v40, v2
	v_mov_b32_e32 v41, v6
	v_pk_mul_f32 v[44:45], v[10:11], v[10:11]
	v_pk_mul_f32 v[46:47], v[8:9], v[8:9]
	v_pk_mul_f32 v[38:39], v[38:39], v[38:39]
	v_pk_mul_f32 v[42:43], v[42:43], v[42:43]
	v_pk_fma_f32 v[14:15], v[14:15], v[126:127], v[50:51]
	v_pk_fma_f32 v[12:13], v[12:13], v[124:125], v[48:49]
	v_pk_mov_b32 v[60:61], v[46:47], v[44:45] op_sel:[1,0]
	v_mov_b32_e32 v47, v45
	v_pk_fma_f32 v[36:37], v[36:37], v[36:37], v[38:39]
	v_pk_fma_f32 v[38:39], v[40:41], v[40:41], v[42:43]
	v_pk_fma_f32 v[18:19], v[18:19], v[130:131], v[54:55]
	v_pk_fma_f32 v[16:17], v[16:17], v[128:129], v[52:53]
	v_mul_f32_e32 v48, v13, v13
	v_mul_f32_e32 v50, v15, v15
	v_pk_add_f32 v[40:41], v[60:61], v[46:47]
	v_pk_add_f32 v[36:37], v[36:37], v[38:39]
	v_mul_f32_e32 v59, v16, v16
	v_mul_f32_e32 v62, v17, v17
	v_mul_f32_e32 v63, v18, v18
	v_mul_f32_e32 v64, v19, v19
	v_pk_fma_f32 v[44:45], v[12:13], v[12:13], v[48:49] op_sel_hi:[1,1,0]
	v_pk_fma_f32 v[48:49], v[14:15], v[14:15], v[50:51] op_sel_hi:[1,1,0]
	v_pk_add_f32 v[38:39], v[40:41], v[40:41] op_sel:[0,1] op_sel_hi:[1,0]
	v_pk_add_f32 v[36:37], v[36:37], v[36:37] op_sel:[0,1] op_sel_hi:[1,0]
	v_pk_mul_f32 v[52:53], v[22:23], v[22:23]
	v_pk_mul_f32 v[54:55], v[20:21], v[20:21]
	v_mov_b32_e32 v45, v63
	v_mov_b32_e32 v49, v64
	v_mov_b32_e32 v39, v62
	v_mov_b32_e32 v37, v59
	v_pk_mov_b32 v[50:51], v[54:55], v[52:53] op_sel:[1,0]
	v_mov_b32_e32 v55, v53
; #define GAS __attribute__((address_space(1)))
; __device__ __forceinline__ void phase12(KP kp, LAS unsigned char* lds, int wave, int bid, int G) {
;     ...
;         const float rstd = 1.0f / sqrtf(wave_sum(s) * (1.0f / DM) + EPS);
;         GAS f32x4* o = (GAS f32x4*)(KOUT() + (size_t)m * DM) + lane;
; #pragma unroll
;         for (int j = 0; j < 8; ++j) o[64 * j] = v[j] * rstd * *(const GAS f32x4*)(fg + 256 * j + 4 * lane);
	v_pk_add_f32 v[40:41], v[44:45], v[48:49]
	v_pk_add_f32 v[36:37], v[36:37], v[38:39]
	v_mul_f32_e32 v56, v25, v25
	v_mul_f32_e32 v58, v27, v27
	v_pk_add_f32 v[42:43], v[50:51], v[54:55]
	v_pk_add_f32 v[36:37], v[36:37], v[40:41]
	v_mul_f32_e32 v65, v32, v32
	v_mul_f32_e32 v66, v33, v33
	v_mul_f32_e32 v67, v34, v34
	v_mul_f32_e32 v103, v35, v35
	v_pk_fma_f32 v[52:53], v[24:25], v[24:25], v[56:57] op_sel_hi:[1,1,0]
	v_pk_fma_f32 v[56:57], v[26:27], v[26:27], v[58:59] op_sel_hi:[1,1,0]
	v_pk_add_f32 v[42:43], v[42:43], v[42:43] op_sel:[0,1] op_sel_hi:[1,0]
	v_pk_add_f32 v[36:37], v[36:37], v[36:37] op_sel:[0,1] op_sel_hi:[1,0]
	v_mov_b32_e32 v53, v67
	v_mov_b32_e32 v57, v103
	v_mov_b32_e32 v43, v66
	v_mov_b32_e32 v37, v65
	v_pk_add_f32 v[44:45], v[52:53], v[56:57]
	v_pk_add_f32 v[36:37], v[36:37], v[42:43]
	s_nop 0
	v_pk_add_f32 v[36:37], v[36:37], v[44:45]
	s_nop 0
	v_add_f32_e32 v36, v36, v37
	s_nop 1
	v_add_f32_dpp v36, v36, v36 quad_perm:[1,0,3,2] row_mask:0xf bank_mask:0xf
	s_nop 1
	v_add_f32_dpp v36, v36, v36 quad_perm:[2,3,0,1] row_mask:0xf bank_mask:0xf
	s_nop 1
	v_add_f32_dpp v36, v36, v36 row_half_mirror row_mask:0xf bank_mask:0xf
	s_nop 1
	v_add_f32_dpp v36, v36, v36 row_mirror row_mask:0xf bank_mask:0xf
	v_mov_b32_e32 v37, v36
	s_nop 1
	v_permlane16_swap_b32_e32 v36, v37
	v_add_f32_e32 v36, v36, v37
	v_mov_b32_e32 v37, v36
	s_nop 1
	v_permlane32_swap_b32_e32 v36, v37
	v_add_f32_e32 v36, v36, v37
	global_load_dwordx4 v[44:47], v[72:73], off offset:1024
	global_load_dwordx4 v[48:51], v[72:73], off offset:2048
	global_load_dwordx4 v[52:55], v[72:73], off offset:3072
	global_load_dwordx4 v[56:59], v[82:83], off
	global_load_dwordx4 v[60:63], v[84:85], off
	global_load_dwordx4 v[64:67], v[86:87], off
	global_load_dwordx4 v[94:97], v[88:89], off
	v_fmamk_f32 v36, v36, 0x3a000000, v101
	v_mul_f32_e32 v37, 0x4f800000, v36
	v_cmp_gt_f32_e32 vcc, s22, v36
	s_nop 1
	v_cndmask_b32_e32 v36, v36, v37, vcc
	v_sqrt_f32_e32 v37, v36
	s_nop 0
	v_add_u32_e32 v38, -1, v37
	v_add_u32_e32 v39, 1, v37
	v_fma_f32 v40, -v38, v37, v36
	v_fma_f32 v41, -v39, v37, v36
	v_cmp_ge_f32_e64 s[0:1], 0, v40
	s_nop 1
	v_cndmask_b32_e64 v37, v37, v38, s[0:1]
	v_cmp_lt_f32_e64 s[0:1], 0, v41
	s_nop 1
	v_cndmask_b32_e64 v37, v37, v39, s[0:1]
	v_mul_f32_e32 v38, 0x37800000, v37
	v_cndmask_b32_e32 v37, v37, v38, vcc
	v_cmp_class_f32_e32 vcc, v36, v102
	s_nop 1
	v_cndmask_b32_e32 v36, v37, v36, vcc
	v_div_scale_f32 v37, s[0:1], v36, v36, 1.0
	v_rcp_f32_e32 v39, v37
	v_div_scale_f32 v38, vcc, 1.0, v36, 1.0
	v_fma_f32 v40, -v37, v39, 1.0
	v_fmac_f32_e32 v39, v40, v39
	v_mul_f32_e32 v40, v38, v39
	v_fma_f32 v41, -v37, v40, v38
	v_fmac_f32_e32 v40, v41, v39
	v_fma_f32 v37, -v37, v40, v38
	v_div_fmas_f32 v37, v37, v39, v40
	v_div_fixup_f32 v36, v37, v36, 1.0
	v_add_co_u32_e32 v38, vcc, s23, v92
	s_nop 1
	v_addc_co_u32_e32 v39, vcc, 0, v93, vcc
	s_waitcnt vmcnt(0)
	v_pk_mul_f32 v[0:1], v[0:1], v[36:37] op_sel_hi:[1,0]
	v_pk_mul_f32 v[2:3], v[2:3], v[36:37] op_sel_hi:[1,0]
	v_pk_mul_f32 v[0:1], v[28:29], v[0:1]
	v_pk_mul_f32 v[2:3], v[30:31], v[2:3]
	global_store_dwordx4 v[92:93], v[0:3], off
	v_pk_mul_f32 v[4:5], v[4:5], v[36:37] op_sel_hi:[1,0]
	v_pk_mul_f32 v[6:7], v[6:7], v[36:37] op_sel_hi:[1,0]
	v_pk_mul_f32 v[4:5], v[44:45], v[4:5]
	v_pk_mul_f32 v[6:7], v[46:47], v[6:7]
	global_store_dwordx4 v[92:93], v[4:7], off offset:1024
	v_pk_mul_f32 v[8:9], v[8:9], v[36:37] op_sel_hi:[1,0]
	v_pk_mul_f32 v[10:11], v[10:11], v[36:37] op_sel_hi:[1,0]
	v_pk_mul_f32 v[8:9], v[48:49], v[8:9]
	v_pk_mul_f32 v[10:11], v[50:51], v[10:11]
	global_store_dwordx4 v[92:93], v[8:11], off offset:2048
	v_pk_mul_f32 v[12:13], v[12:13], v[36:37] op_sel_hi:[1,0]
	v_pk_mul_f32 v[14:15], v[14:15], v[36:37] op_sel_hi:[1,0]
	v_pk_mul_f32 v[12:13], v[52:53], v[12:13]
	v_pk_mul_f32 v[14:15], v[54:55], v[14:15]
	global_store_dwordx4 v[92:93], v[12:15], off offset:3072
	v_pk_mul_f32 v[16:17], v[16:17], v[36:37] op_sel_hi:[1,0]
	v_pk_mul_f32 v[18:19], v[18:19], v[36:37] op_sel_hi:[1,0]
	v_pk_mul_f32 v[16:17], v[56:57], v[16:17]
	v_pk_mul_f32 v[18:19], v[58:59], v[18:19]
	global_store_dwordx4 v[38:39], v[16:19], off
	v_pk_mul_f32 v[20:21], v[20:21], v[36:37] op_sel_hi:[1,0]
	v_pk_mul_f32 v[22:23], v[22:23], v[36:37] op_sel_hi:[1,0]
	v_pk_mul_f32 v[20:21], v[60:61], v[20:21]
	v_pk_mul_f32 v[22:23], v[62:63], v[22:23]
	global_store_dwordx4 v[38:39], v[20:23], off offset:1024
	v_pk_mul_f32 v[24:25], v[24:25], v[36:37] op_sel_hi:[1,0]
	v_pk_mul_f32 v[26:27], v[26:27], v[36:37] op_sel_hi:[1,0]
	v_pk_mul_f32 v[24:25], v[64:65], v[24:25]
	v_pk_mul_f32 v[26:27], v[66:67], v[26:27]
	global_store_dwordx4 v[38:39], v[24:27], off offset:2048
	v_pk_mul_f32 v[32:33], v[32:33], v[36:37] op_sel_hi:[1,0]
	v_pk_mul_f32 v[34:35], v[34:35], v[36:37] op_sel_hi:[1,0]
	v_pk_mul_f32 v[32:33], v[94:95], v[32:33]
	v_pk_mul_f32 v[34:35], v[96:97], v[34:35]
	global_store_dwordx4 v[38:39], v[32:35], off offset:3072
	s_cbranch_scc1 .LBB0_4682
